# odd-layer QKV GEMM tile head: row-scale table entry by LDS-DMA as well
# baseline (speedup 1.0000x reference)
; template <class Epi, bool ALIGN_EPI, bool SP2>
; __device__ __forceinline__ void gemm_phase(LAS unsigned char* lds, LAS float* tab, const Gemm g, const StaticOrder& S, const Epi& E, int wave_s) {
;     ...
;         const bool has_next = S.next(ui + 1, nxt);
;         if constexpr (Epi::NEED_RSTD) {
;             if (Epi::I8) { if (tid < 256) tab[(ui & 1) * 256 + tid] = g.ssp[(size_t)cur.pm * BM + tid]; }
;             else if (tid < 256) { const f32x4* p = (const f32x4*)(g.ssp + ((size_t)cur.pm * BM + tid) * 16); const f32x4 a = p[0], b = p[1], c = p[2], d = p[3];
;                 const float s = ((a[0] + a[1]) + (a[2] + a[3])) + ((b[0] + b[1]) + (b[2] + b[3])) + ((c[0] + c[1]) + (c[2] + c[3])) + ((d[0] + d[1]) + (d[2] + d[3]));
;                 tab[(ui & 1) * 256 + tid] = rsqrtf(s * (1.0f / D) + EPS); }
.LBB0_285:
	s_and_saveexec_b64 s[18:19], s[6:7]
	s_cbranch_execz .LBB0_287
	s_ashr_i32 s5, s4, 31
	s_lshl_b64 s[2:3], s[4:5], 10
	v_lshl_add_u64 v[2:3], v[138:139], 0, s[2:3]
	s_lshl_b32 s2, s0, 10
	s_and_b32 s2, s2, 0x400
	v_readfirstlane_b32 s3, v189
	s_mov_b32 s5, m0
	s_add_i32 s2, s2, s3
	s_mov_b32 m0, s2
	s_nop 0
	global_load_lds_dword v[2:3], off
	s_mov_b32 m0, s5
